# prologue weight copies stored write-through; barrier after E(0) skips the L2 write-back too
# baseline (speedup 1.0000x reference)
; __device__ void wconv_loop(const Params& p, int l, int first, int end, int stride, char* smem, int oz) {
;     ...
;     for (int idt = first; idt < end; idt += stride) {
;         int id = idt;
;         const bool isin = id < 16 * 27;
;         if (!isin) id -= 16 * 27;
;         const int NN = isin ? INW : DM;
;         const int ntn = isin ? 27 : 8;
;         const int k0 = (id / ntn) * 64, n0 = (id % ntn) * 128;
;         bf16_t* Wt = (bf16_t*)(p.ws + (isin ? OFF_WINT : OFF_WOUTT + (size_t)(l & 1) * SZ_WOUTT));
;         float4 v[4];
; #pragma unroll
;         for (int i = 0; i < 4; ++i) v[i] = vn[i];
;         if (idt + stride < end) WC_LOAD(idt + stride)
;         __syncthreads();
; #pragma unroll
;         for (int i = 0; i < 4; ++i) {
;             const int pc = tid + 512 * i, r = pc >> 5, c4 = (pc & 31) * 4;
;             tile[r * 129 + c4] = v[i].x; tile[r * 129 + c4 + 1] = v[i].y; tile[r * 129 + c4 + 2] = v[i].z; tile[r * 129 + c4 + 3] = v[i].w;
;         }
;         __syncthreads();
;         {
;             const int nn = tid >> 2, q = tid & 3, n = n0 + nn;
;             if (n < NN) {
;                 u32x4 o0, o1;
; #pragma unroll
;                 for (int w = 0; w < 4; ++w) {
;                     o0[w] = cvt_pk(tile[(q * 16 + 2 * w) * 129 + nn], tile[(q * 16 + 2 * w + 1) * 129 + nn]);
;                     o1[w] = cvt_pk(tile[(q * 16 + 8 + 2 * w) * 129 + nn], tile[(q * 16 + 8 + 2 * w + 1) * 129 + nn]);
;                 }
;                 *(u32x4*)(Wt + (size_t)n * 1024 + k0 + q * 16) = o0;
;                 *(u32x4*)(Wt + (size_t)n * 1024 + k0 + q * 16 + 8) = o1;
;             }
.LBB0_230:
	s_add_i32 s28, s3, 0xfffffe50
	s_cmpk_lt_i32 s3, 0x1b0
	s_cselect_b64 s[36:37], -1, 0
	s_and_b64 s[26:27], s[36:37], exec
	s_cselect_b32 s26, 27, 8
	v_cvt_f32_ubyte0_e32 v2, s26
	v_rcp_iflag_f32_e32 v2, v2
	s_cselect_b32 s27, s3, s28
	s_movk_i32 s3, 0xd10
	s_cselect_b32 s28, s3, 0x400
	v_mul_f32_e32 v2, 0x4f7ffffe, v2
	v_cvt_u32_f32_e32 v2, v2
	s_sub_i32 s31, 0, s26
	s_abs_i32 s29, s27
	s_ashr_i32 s3, s27, 31
	v_readfirstlane_b32 s38, v2
	s_mul_i32 s31, s31, s38
	s_mul_hi_u32 s31, s38, s31
	s_add_i32 s38, s38, s31
	s_mul_hi_u32 s31, s29, s38
	s_mul_i32 s38, s31, s26
	s_sub_i32 s29, s29, s38
	s_add_i32 s39, s31, 1
	s_sub_i32 s38, s29, s26
	s_cmp_ge_u32 s29, s26
	s_cselect_b32 s31, s39, s31
	s_cselect_b32 s29, s38, s29
	s_add_i32 s38, s31, 1
	s_cmp_ge_u32 s29, s26
	s_cselect_b32 s29, s38, s31
	s_xor_b32 s29, s29, s3
	v_add_u32_e32 v2, 0x2040, v45
	s_sub_i32 s3, s29, s3
	s_barrier
	ds_write2_b32 v45, v8, v9 offset1:1
	ds_write2_b32 v45, v10, v11 offset0:2 offset1:3
	ds_write2_b32 v2, v4, v5 offset1:1
	v_add_u32_e32 v2, 0x2048, v45
	s_mul_i32 s26, s3, s26
	ds_write2_b32 v2, v6, v7 offset1:1
	v_add_u32_e32 v2, 0x4080, v45
	s_sub_i32 s26, s27, s26
	ds_write2_b32 v2, v12, v13 offset1:1
	v_add_u32_e32 v2, 0x4088, v45
	ds_write2_b32 v2, v14, v15 offset1:1
	v_add_u32_e32 v2, 0x60c0, v45
	v_lshl_or_b32 v4, s26, 7, v39
	ds_write2_b32 v2, v24, v25 offset1:1
	v_add_u32_e32 v2, 0x60c8, v45
	v_cmp_gt_i32_e32 vcc, s28, v4
	ds_write2_b32 v2, v26, v27 offset1:1
	s_waitcnt lgkmcnt(0)
	s_barrier
	s_and_saveexec_b64 s[28:29], vcc
	s_cbranch_execz .LBB0_219
	ds_read_b32 v2, v40
	ds_read_b32 v5, v41 offset:516
	s_and_b64 s[26:27], s[36:37], exec
	s_mov_b32 s26, 0x80000
	s_cselect_b32 s26, s26, 0x780000
	s_lshl_b32 s36, s3, 6
	s_waitcnt lgkmcnt(0)
	v_cvt_pk_bf16_f32 v6, v2, v5
	v_add_u32_e32 v2, 0xe00, v41
	ds_read2_b32 v[14:15], v2 offset0:7 offset1:136
	v_add_u32_e32 v2, 0x1200, v41
	ds_read2_b32 v[8:9], v2 offset0:9 offset1:138
	ds_read_b32 v2, v40 offset:1032
	ds_read_b32 v5, v41 offset:1548
	s_add_u32 s38, s60, s26
	s_addc_u32 s39, s61, 0
	s_ashr_i32 s37, s36, 31
	s_waitcnt lgkmcnt(2)
	v_cvt_pk_bf16_f32 v10, v15, v8
	s_waitcnt lgkmcnt(0)
	v_cvt_pk_bf16_f32 v7, v2, v5
	v_add_u32_e32 v2, 0x1600, v41
	ds_read2_b32 v[12:13], v2 offset0:11 offset1:140
	ds_read_b32 v2, v40 offset:2064
	ds_read_b32 v5, v41 offset:2580
	v_mov_b32_e32 v37, v3
	s_waitcnt lgkmcnt(2)
	v_cvt_pk_bf16_f32 v11, v9, v12
	s_waitcnt lgkmcnt(0)
	v_cvt_pk_bf16_f32 v8, v2, v5
	v_add_u32_e32 v2, 0x1a00, v41
	ds_read2_b32 v[24:25], v2 offset0:13 offset1:142
	ds_read_b32 v2, v40 offset:3096
	v_ashrrev_i32_e32 v5, 31, v4
	v_lshlrev_b64 v[4:5], 11, v[4:5]
	v_lshl_add_u64 v[4:5], s[38:39], 0, v[4:5]
	v_lshl_add_u64 v[4:5], s[36:37], 1, v[4:5]
	s_waitcnt lgkmcnt(0)
	v_cvt_pk_bf16_f32 v9, v2, v14
	ds_read_b32 v2, v41 offset:7740
	v_lshl_add_u64 v[4:5], v[4:5], 0, v[36:37]
	v_cvt_pk_bf16_f32 v12, v13, v24
	s_waitcnt lgkmcnt(0)
	v_cvt_pk_bf16_f32 v13, v25, v2
	global_store_dwordx4 v[4:5], v[6:9], off sc1
	global_store_dwordx4 v[4:5], v[10:13], off offset:16 sc1
	s_branch .LBB0_219

; __device__ __forceinline__ unsigned xb_add(unsigned* p, unsigned v) { return __hip_atomic_fetch_add(p, v, __ATOMIC_RELAXED, __HIP_MEMORY_SCOPE_AGENT); }
; __device__ __forceinline__ void xcd_barrier(const XcdBarrier& b) {
;     ...
;         const unsigned old = xb_add(&bar[XB_XSUB(b.x)], 1u);
;         const unsigned gen = old / nloc;
;         if (old + 1u == (gen + 1u) * nloc) {
;             __builtin_amdgcn_fence(__ATOMIC_RELEASE, "agent");
;             asm volatile("s_waitcnt vmcnt(0)" ::: "memory");
;             const unsigned og = xb_add(&bar[XB_TOP], 1u);
.LBB0_1009:
	s_andn2_saveexec_b64 s[2:3], s[2:3]
	s_cbranch_execz .LBB0_1029
	s_mov_b64 s[2:3], exec
	v_readlane_b32 s24, v255, 35
	s_nop 3
	s_cmp_eq_u32 s24, 0
	s_cbranch_scc1 .Lxb_nowb
	s_cmp_eq_u32 s24, 6
	s_cbranch_scc1 .Lxb_nowb
	s_cmp_eq_u32 s24, 12
	s_cbranch_scc1 .Lxb_nowb
	s_cmp_eq_u32 s24, 18
	s_cbranch_scc1 .Lxb_nowb
	buffer_wbl2 sc1
